# mixer-phase converter variant: row-contiguous 1 KB loads per instruction and 16-byte stores (same conversion), rest unchanged
# speedup vs baseline: 1.0010x; 1.0010x over previous
.LBB0_486:
	s_or_b64 exec, exec, s[8:9]
	v_readlane_b32 s33, v255, 12
	s_cmpk_lt_u32 s33, 192
	s_cbranch_scc1 .Lfc_p3_skip
	v_lshrrev_b32_e32 v1, 6, v0
	v_lshlrev_b32_e32 v1, 4, v1
	v_and_b32_e32 v2, 31, v0
	v_lshlrev_b32_e32 v2, 4, v2
	v_mov_b32_e32 v3, 0
	v_and_b32_e32 v18, 32, v0
	v_and_b32_e32 v4, 3, v0
	v_lshlrev_b32_e32 v4, 5, v4
	v_mov_b32_e32 v5, 0
	v_lshrrev_b32_e32 v17, 2, v0
	v_and_b32_e32 v6, 31, v17
	v_lshlrev_b32_e32 v6, 2, v6
	v_lshrrev_b32_e32 v12, 5, v17
	v_add_u32_e32 v6, v6, v12
	v_mul_u32_u24_e32 v17, 0x84, v17
	v_add_u32_e32 v17, v17, v4
	v_mov_b32_e32 v7, 2
	v_mov_b32_e32 v8, 0x42800000
	v_mov_b32_e32 v9, 0x42800000
	v_and_b32_e32 v16, 31, v0
	v_mul_u32_u24_e32 v16, 0x84, v16
	v_add_u32_e32 v16, v16, v1
	v_bfe_u32 v12, v0, 5, 1
	v_mul_u32_u24_e32 v12, 0x4200, v12
	v_add_u32_e32 v16, v16, v12
	v_mov_b32_e32 v13, 0x25a00
	v_readlane_b32 s56, v255, 5
	v_readlane_b32 s57, v255, 6
	v_readlane_b32 s13, v255, 7
	v_readlane_b32 s8, v255, 14
	v_readlane_b32 s9, v255, 15
	v_readlane_b32 s33, v255, 18
	s_load_dwordx2 s[36:37], s[8:9], 0x30
	s_load_dwordx2 s[38:39], s[8:9], 0x48
	s_load_dwordx4 s[40:43], s[8:9], 0x78
	s_load_dwordx2 s[44:45], s[8:9], 0x88
	s_add_u32 s58, s56, 0x5000
	s_addc_u32 s59, s57, 0
	s_lshl_b32 s33, s33, 10
	s_add_i32 s33, s33, 512
	s_add_u32 s60, s58, s33
	s_addc_u32 s61, s59, 0
	s_waitcnt lgkmcnt(0)
	v_cmp_eq_u32_e32 vcc, 0, v0
	s_and_saveexec_b64 s[16:17], vcc
	s_cbranch_execz .Lfc_p3_init_done
	global_load_dword v11, v195, s[60:61] sc1
	s_mov_b32 s14, -1
	s_mov_b32 s25, -1
	s_waitcnt vmcnt(0)
	v_readfirstlane_b32 s33, v11
	s_cmp_ge_u32 s33, s13
	s_cbranch_scc1 .Lfc_p3_init_w
	v_mov_b32_e32 v12, 4
	global_atomic_add v10, v195, v12, s[58:59] sc0
	s_waitcnt vmcnt(0)
	v_readfirstlane_b32 s33, v10
	s_cmpk_lt_u32 s33, 0x4c40
	s_cselect_b32 s14, s33, -1
	s_add_i32 s33, s33, 2
	s_cmpk_lt_u32 s33, 0x4c40
	s_cselect_b32 s25, s33, -1

.Lfc_p3_pro_s0_kfin:
	s_lshl_b32 s9, s9, 9
	s_add_u32 s18, s18, s9
	s_add_u32 s62, s62, s18
	s_addc_u32 s63, s63, 0
	s_lshl_b32 s8, s8, 7
	s_add_u32 s19, s19, s8
	s_add_u32 s64, s56, s19
	s_addc_u32 s65, s57, 0
	v_mov_b32_e32 v14, s62
	v_mov_b32_e32 v15, s63
	v_mov_b32_e32 v22, s64
	v_mov_b32_e32 v23, s65
	v_lshl_add_u64 v[22:23], v[22:23], 0, v[4:5]
	v_mad_u64_u32 v[28:29], vcc, v6, s10, v[22:23]
	s_and_b32 s35, s14, 0x3fffffff
	s_add_i32 s35, s35, 1
	s_cmpk_ge_u32 s35, 0x2620
	s_cselect_b32 s33, 1, 0
	s_mul_i32 s8, s33, 0x2620
	s_sub_u32 s35, s35, s8
	s_cmpk_lt_u32 s35, 0x420
	s_cbranch_scc1 .Lfc_p3_pro_s1_kin
	s_cmpk_lt_u32 s35, 0x520
	s_cbranch_scc1 .Lfc_p3_pro_s1_kout
	s_cmpk_lt_u32 s35, 0x1b20
	s_cbranch_scc1 .Lfc_p3_pro_s1_kgu
	s_sub_u32 s35, s35, 0x1b20
	s_mul_i32 s8, s35, 0xba2f
	s_lshr_b32 s8, s8, 23
	s_mul_i32 s9, s8, 0xb0
	s_sub_u32 s35, s35, s9
	s_lshl_b32 s33, s33, 4
	s_add_i32 s33, s33, s8
	s_lshr_b32 s8, s35, 1
	s_mul_i32 s9, s8, 0xbb
	s_lshr_b32 s9, s9, 11
	s_mul_i32 s18, s9, 11
	s_sub_u32 s8, s8, s18
	s_lshl_b32 s9, s9, 1
	s_and_b32 s35, s35, 1
	s_or_b32 s9, s9, s35
	s_mov_b64 s[62:63], s[44:45]
	s_movk_i32 s2, 0x2000
	s_movk_i32 s10, 0x600
	s_mul_i32 s18, s33, 0xb00000
	s_mul_i32 s19, s8, 0x100000
	s_add_u32 s18, s18, s19
	s_mul_i32 s19, s33, 0x300000
	s_add_u32 s19, s19, 0x1b300000
	s_mul_i32 s35, s9, 0x30000
	s_add_u32 s19, s19, s35
	s_branch .Lfc_p3_pro_s1_kfin

.Lfc_p3_pro_s1_kfin:
	s_lshl_b32 s9, s9, 9
	s_add_u32 s18, s18, s9
	s_add_u32 s62, s62, s18
	s_addc_u32 s63, s63, 0
	s_lshl_b32 s8, s8, 7
	s_add_u32 s19, s19, s8
	s_add_u32 s64, s56, s19
	s_addc_u32 s65, s57, 0
	v_mov_b32_e32 v12, s62
	v_mov_b32_e32 v19, s63
	v_cmp_ne_u32_e32 vcc, 0, v18
	s_nop 1
	v_cndmask_b32_e32 v14, v14, v12, vcc
	v_cndmask_b32_e32 v15, v15, v19, vcc
	v_mov_b32_e32 v22, s64
	v_mov_b32_e32 v23, s65
	v_lshl_add_u64 v[22:23], v[22:23], 0, v[4:5]
	v_mad_u64_u32 v[30:31], vcc, v6, s10, v[22:23]
	v_lshl_add_u64 v[14:15], v[14:15], 0, v[2:3]
	v_mad_u64_u32 v[20:21], vcc, v1, s2, v[14:15]
	global_load_dwordx4 v[48:51], v[20:21], off nt
	v_lshl_add_u64 v[20:21], v[20:21], 0, s[2:3]
	global_load_dwordx4 v[52:55], v[20:21], off nt
	v_lshl_add_u64 v[20:21], v[20:21], 0, s[2:3]
	global_load_dwordx4 v[56:59], v[20:21], off nt
	v_lshl_add_u64 v[20:21], v[20:21], 0, s[2:3]
	global_load_dwordx4 v[60:63], v[20:21], off nt
	v_lshl_add_u64 v[20:21], v[20:21], 0, s[2:3]
	global_load_dwordx4 v[64:67], v[20:21], off nt
	v_lshl_add_u64 v[20:21], v[20:21], 0, s[2:3]
	global_load_dwordx4 v[68:71], v[20:21], off nt
	v_lshl_add_u64 v[20:21], v[20:21], 0, s[2:3]
	global_load_dwordx4 v[72:75], v[20:21], off nt
	v_lshl_add_u64 v[20:21], v[20:21], 0, s[2:3]
	global_load_dwordx4 v[76:79], v[20:21], off nt
	v_lshl_add_u64 v[20:21], v[20:21], 0, s[2:3]
	global_load_dwordx4 v[80:83], v[20:21], off nt
	v_lshl_add_u64 v[20:21], v[20:21], 0, s[2:3]
	global_load_dwordx4 v[84:87], v[20:21], off nt
	v_lshl_add_u64 v[20:21], v[20:21], 0, s[2:3]
	global_load_dwordx4 v[88:91], v[20:21], off nt
	v_lshl_add_u64 v[20:21], v[20:21], 0, s[2:3]
	global_load_dwordx4 v[92:95], v[20:21], off nt
	v_lshl_add_u64 v[20:21], v[20:21], 0, s[2:3]
	global_load_dwordx4 v[96:99], v[20:21], off nt
	v_lshl_add_u64 v[20:21], v[20:21], 0, s[2:3]
	global_load_dwordx4 v[100:103], v[20:21], off nt
	v_lshl_add_u64 v[20:21], v[20:21], 0, s[2:3]
	global_load_dwordx4 v[104:107], v[20:21], off nt
	v_lshl_add_u64 v[20:21], v[20:21], 0, s[2:3]
	global_load_dwordx4 v[108:111], v[20:21], off nt

.Lfc_p3_st0_s0_kfin:
	s_lshl_b32 s9, s9, 9
	s_add_u32 s18, s18, s9
	s_add_u32 s62, s62, s18
	s_addc_u32 s63, s63, 0
	s_lshl_b32 s8, s8, 7
	s_add_u32 s19, s19, s8
	s_add_u32 s64, s56, s19
	s_addc_u32 s65, s57, 0
	v_mov_b32_e32 v14, s62
	v_mov_b32_e32 v15, s63
	v_mov_b32_e32 v22, s64
	v_mov_b32_e32 v23, s65
	v_lshl_add_u64 v[22:23], v[22:23], 0, v[4:5]
	v_mad_u64_u32 v[32:33], vcc, v6, s10, v[22:23]
	s_and_b32 s35, s25, 0x3fffffff
	s_add_i32 s35, s35, 1
	s_cmpk_ge_u32 s35, 0x2620
	s_cselect_b32 s33, 1, 0
	s_mul_i32 s8, s33, 0x2620
	s_sub_u32 s35, s35, s8
	s_cmpk_lt_u32 s35, 0x420
	s_cbranch_scc1 .Lfc_p3_st0_s1_kin
	s_cmpk_lt_u32 s35, 0x520
	s_cbranch_scc1 .Lfc_p3_st0_s1_kout
	s_cmpk_lt_u32 s35, 0x1b20
	s_cbranch_scc1 .Lfc_p3_st0_s1_kgu
	s_sub_u32 s35, s35, 0x1b20
	s_mul_i32 s8, s35, 0xba2f
	s_lshr_b32 s8, s8, 23
	s_mul_i32 s9, s8, 0xb0
	s_sub_u32 s35, s35, s9
	s_lshl_b32 s33, s33, 4
	s_add_i32 s33, s33, s8
	s_lshr_b32 s8, s35, 1
	s_mul_i32 s9, s8, 0xbb
	s_lshr_b32 s9, s9, 11
	s_mul_i32 s18, s9, 11
	s_sub_u32 s8, s8, s18
	s_lshl_b32 s9, s9, 1
	s_and_b32 s35, s35, 1
	s_or_b32 s9, s9, s35
	s_mov_b64 s[62:63], s[44:45]
	s_movk_i32 s2, 0x2000
	s_movk_i32 s10, 0x600
	s_mul_i32 s18, s33, 0xb00000
	s_mul_i32 s19, s8, 0x100000
	s_add_u32 s18, s18, s19
	s_mul_i32 s19, s33, 0x300000
	s_add_u32 s19, s19, 0x1b300000
	s_mul_i32 s35, s9, 0x30000
	s_add_u32 s19, s19, s35
	s_branch .Lfc_p3_st0_s1_kfin

.Lfc_p3_st0_s1_kfin:
	s_lshl_b32 s9, s9, 9
	s_add_u32 s18, s18, s9
	s_add_u32 s62, s62, s18
	s_addc_u32 s63, s63, 0
	s_lshl_b32 s8, s8, 7
	s_add_u32 s19, s19, s8
	s_add_u32 s64, s56, s19
	s_addc_u32 s65, s57, 0
	v_mov_b32_e32 v12, s62
	v_mov_b32_e32 v19, s63
	v_cmp_ne_u32_e32 vcc, 0, v18
	s_nop 1
	v_cndmask_b32_e32 v14, v14, v12, vcc
	v_cndmask_b32_e32 v15, v15, v19, vcc
	v_mov_b32_e32 v22, s64
	v_mov_b32_e32 v23, s65
	v_lshl_add_u64 v[22:23], v[22:23], 0, v[4:5]
	v_mad_u64_u32 v[34:35], vcc, v6, s10, v[22:23]
	v_lshl_add_u64 v[14:15], v[14:15], 0, v[2:3]
	v_mad_u64_u32 v[20:21], vcc, v1, s2, v[14:15]
	global_load_dwordx4 v[112:115], v[20:21], off nt
	v_lshl_add_u64 v[20:21], v[20:21], 0, s[2:3]
	global_load_dwordx4 v[116:119], v[20:21], off nt
	v_lshl_add_u64 v[20:21], v[20:21], 0, s[2:3]
	global_load_dwordx4 v[120:123], v[20:21], off nt
	v_lshl_add_u64 v[20:21], v[20:21], 0, s[2:3]
	global_load_dwordx4 v[124:127], v[20:21], off nt
	v_lshl_add_u64 v[20:21], v[20:21], 0, s[2:3]
	global_load_dwordx4 v[128:131], v[20:21], off nt
	v_lshl_add_u64 v[20:21], v[20:21], 0, s[2:3]
	global_load_dwordx4 v[132:135], v[20:21], off nt
	v_lshl_add_u64 v[20:21], v[20:21], 0, s[2:3]
	global_load_dwordx4 v[136:139], v[20:21], off nt
	v_lshl_add_u64 v[20:21], v[20:21], 0, s[2:3]
	global_load_dwordx4 v[140:143], v[20:21], off nt
	v_lshl_add_u64 v[20:21], v[20:21], 0, s[2:3]
	global_load_dwordx4 v[144:147], v[20:21], off nt
	v_lshl_add_u64 v[20:21], v[20:21], 0, s[2:3]
	global_load_dwordx4 v[148:151], v[20:21], off nt
	v_lshl_add_u64 v[20:21], v[20:21], 0, s[2:3]
	global_load_dwordx4 v[152:155], v[20:21], off nt
	v_lshl_add_u64 v[20:21], v[20:21], 0, s[2:3]
	global_load_dwordx4 v[156:159], v[20:21], off nt
	v_lshl_add_u64 v[20:21], v[20:21], 0, s[2:3]
	global_load_dwordx4 v[160:163], v[20:21], off nt
	v_lshl_add_u64 v[20:21], v[20:21], 0, s[2:3]
	global_load_dwordx4 v[164:167], v[20:21], off nt
	v_lshl_add_u64 v[20:21], v[20:21], 0, s[2:3]
	global_load_dwordx4 v[168:171], v[20:21], off nt
	v_lshl_add_u64 v[20:21], v[20:21], 0, s[2:3]
	global_load_dwordx4 v[172:175], v[20:21], off nt
	s_waitcnt vmcnt(16)
	s_branch .Lfc_p3_st0_cvt

.Lfc_p3_st0_cvt:
	v_pk_mul_f32 v[48:49], v[48:49], v[8:9]
	v_pk_mul_f32 v[50:51], v[50:51], v[8:9]
	v_pk_mul_f32 v[52:53], v[52:53], v[8:9]
	v_pk_mul_f32 v[54:55], v[54:55], v[8:9]
	v_cvt_pk_fp8_f32 v48, v48, v52
	v_cvt_pk_fp8_f32 v49, v49, v53
	v_cvt_pk_fp8_f32 v50, v50, v54
	v_cvt_pk_fp8_f32 v51, v51, v55
	ds_write_b16 v16, v48 offset:0
	ds_write_b16 v16, v49 offset:4224
	ds_write_b16 v16, v50 offset:8448
	ds_write_b16 v16, v51 offset:12672
	v_pk_mul_f32 v[56:57], v[56:57], v[8:9]
	v_pk_mul_f32 v[58:59], v[58:59], v[8:9]
	v_pk_mul_f32 v[60:61], v[60:61], v[8:9]
	v_pk_mul_f32 v[62:63], v[62:63], v[8:9]
	v_cvt_pk_fp8_f32 v56, v56, v60
	v_cvt_pk_fp8_f32 v57, v57, v61
	v_cvt_pk_fp8_f32 v58, v58, v62
	v_cvt_pk_fp8_f32 v59, v59, v63
	ds_write_b16 v16, v56 offset:2
	ds_write_b16 v16, v57 offset:4226
	ds_write_b16 v16, v58 offset:8450
	ds_write_b16 v16, v59 offset:12674
	v_pk_mul_f32 v[64:65], v[64:65], v[8:9]
	v_pk_mul_f32 v[66:67], v[66:67], v[8:9]
	v_pk_mul_f32 v[68:69], v[68:69], v[8:9]
	v_pk_mul_f32 v[70:71], v[70:71], v[8:9]
	v_cvt_pk_fp8_f32 v64, v64, v68
	v_cvt_pk_fp8_f32 v65, v65, v69
	v_cvt_pk_fp8_f32 v66, v66, v70
	v_cvt_pk_fp8_f32 v67, v67, v71
	ds_write_b16 v16, v64 offset:4
	ds_write_b16 v16, v65 offset:4228
	ds_write_b16 v16, v66 offset:8452
	ds_write_b16 v16, v67 offset:12676
	v_pk_mul_f32 v[72:73], v[72:73], v[8:9]
	v_pk_mul_f32 v[74:75], v[74:75], v[8:9]
	v_pk_mul_f32 v[76:77], v[76:77], v[8:9]
	v_pk_mul_f32 v[78:79], v[78:79], v[8:9]
	v_cvt_pk_fp8_f32 v72, v72, v76
	v_cvt_pk_fp8_f32 v73, v73, v77
	v_cvt_pk_fp8_f32 v74, v74, v78
	v_cvt_pk_fp8_f32 v75, v75, v79
	ds_write_b16 v16, v72 offset:6
	ds_write_b16 v16, v73 offset:4230
	ds_write_b16 v16, v74 offset:8454
	ds_write_b16 v16, v75 offset:12678
	v_pk_mul_f32 v[80:81], v[80:81], v[8:9]
	v_pk_mul_f32 v[82:83], v[82:83], v[8:9]
	v_pk_mul_f32 v[84:85], v[84:85], v[8:9]
	v_pk_mul_f32 v[86:87], v[86:87], v[8:9]
	v_cvt_pk_fp8_f32 v80, v80, v84
	v_cvt_pk_fp8_f32 v81, v81, v85
	v_cvt_pk_fp8_f32 v82, v82, v86
	v_cvt_pk_fp8_f32 v83, v83, v87
	ds_write_b16 v16, v80 offset:8
	ds_write_b16 v16, v81 offset:4232
	ds_write_b16 v16, v82 offset:8456
	ds_write_b16 v16, v83 offset:12680
	v_pk_mul_f32 v[88:89], v[88:89], v[8:9]
	v_pk_mul_f32 v[90:91], v[90:91], v[8:9]
	v_pk_mul_f32 v[92:93], v[92:93], v[8:9]
	v_pk_mul_f32 v[94:95], v[94:95], v[8:9]
	v_cvt_pk_fp8_f32 v88, v88, v92
	v_cvt_pk_fp8_f32 v89, v89, v93
	v_cvt_pk_fp8_f32 v90, v90, v94
	v_cvt_pk_fp8_f32 v91, v91, v95
	ds_write_b16 v16, v88 offset:10
	ds_write_b16 v16, v89 offset:4234
	ds_write_b16 v16, v90 offset:8458
	ds_write_b16 v16, v91 offset:12682
	v_pk_mul_f32 v[96:97], v[96:97], v[8:9]
	v_pk_mul_f32 v[98:99], v[98:99], v[8:9]
	v_pk_mul_f32 v[100:101], v[100:101], v[8:9]
	v_pk_mul_f32 v[102:103], v[102:103], v[8:9]
	v_cvt_pk_fp8_f32 v96, v96, v100
	v_cvt_pk_fp8_f32 v97, v97, v101
	v_cvt_pk_fp8_f32 v98, v98, v102
	v_cvt_pk_fp8_f32 v99, v99, v103
	ds_write_b16 v16, v96 offset:12
	ds_write_b16 v16, v97 offset:4236
	ds_write_b16 v16, v98 offset:8460
	ds_write_b16 v16, v99 offset:12684
	v_pk_mul_f32 v[104:105], v[104:105], v[8:9]
	v_pk_mul_f32 v[106:107], v[106:107], v[8:9]
	v_pk_mul_f32 v[108:109], v[108:109], v[8:9]
	v_pk_mul_f32 v[110:111], v[110:111], v[8:9]
	v_cvt_pk_fp8_f32 v104, v104, v108
	v_cvt_pk_fp8_f32 v105, v105, v109
	v_cvt_pk_fp8_f32 v106, v106, v110
	v_cvt_pk_fp8_f32 v107, v107, v111
	ds_write_b16 v16, v104 offset:14
	ds_write_b16 v16, v105 offset:4238
	ds_write_b16 v16, v106 offset:8462
	ds_write_b16 v16, v107 offset:12686
	v_cmp_eq_u32_e32 vcc, 0, v0
	s_and_saveexec_b64 s[16:17], vcc
	s_cbranch_execz .Lfc_p3_st0_slot_done
	s_mov_b32 s33, -1
	s_cmp_lt_i32 s25, 0
	s_cbranch_scc1 .Lfc_p3_st0_slot_w
	s_bitcmp1_b32 s25, 30
	s_cbranch_scc1 .Lfc_p3_st0_slot_w
	v_readfirstlane_b32 s35, v10
	v_readfirstlane_b32 s8, v11
	s_cmpk_ge_u32 s35, 0x4c40
	s_cbranch_scc1 .Lfc_p3_st0_slot_w
	s_cmp_ge_u32 s8, s13
	s_cselect_b32 s8, 0x40000000, 0
	s_or_b32 s33, s35, s8

.Lfc_p3_st0_slot_done:
	s_or_b64 exec, exec, s[16:17]
	s_waitcnt lgkmcnt(0)
	s_barrier
	ds_read_b32 v12, v13 offset:0
	v_add_u32_e32 v176, 0x0, v17
	ds_read2_b32 v[178:179], v176 offset0:0 offset1:1
	ds_read2_b32 v[180:181], v176 offset0:2 offset1:3
	ds_read2_b32 v[182:183], v176 offset0:4 offset1:5
	ds_read2_b32 v[184:185], v176 offset0:6 offset1:7
	v_add_u32_e32 v186, 0x4200, v17
	ds_read2_b32 v[36:37], v186 offset0:0 offset1:1
	ds_read2_b32 v[38:39], v186 offset0:2 offset1:3
	ds_read2_b32 v[40:41], v186 offset0:4 offset1:5
	ds_read2_b32 v[42:43], v186 offset0:6 offset1:7
	s_waitcnt lgkmcnt(4)
	global_store_dwordx4 v[28:29], v[178:181], off
	global_store_dwordx4 v[28:29], v[182:185], off offset:16
	s_waitcnt lgkmcnt(0)
	global_store_dwordx4 v[30:31], v[36:39], off
	global_store_dwordx4 v[30:31], v[40:43], off offset:16
	s_waitcnt lgkmcnt(0)
	s_mov_b32 s14, s25
	v_readfirstlane_b32 s25, v12
	s_cmp_lt_i32 s14, 0
	s_cbranch_scc1 .Lfc_p3_exit
	s_cmp_lt_i32 s25, 0
	s_cbranch_scc1 .Lfc_p3_st1_nonext
	s_bitcmp1_b32 s25, 30
	s_cbranch_scc1 .Lfc_p3_st1_noclaim
	v_cmp_eq_u32_e32 vcc, 0, v0
	s_and_saveexec_b64 s[16:17], vcc
	s_cbranch_execz .Lfc_p3_st1_claimed
	global_atomic_add v10, v195, v7, s[58:59] sc0
	global_load_dword v11, v195, s[60:61] sc1

.Lfc_p3_st1_s0_kfin:
	s_lshl_b32 s9, s9, 9
	s_add_u32 s18, s18, s9
	s_add_u32 s62, s62, s18
	s_addc_u32 s63, s63, 0
	s_lshl_b32 s8, s8, 7
	s_add_u32 s19, s19, s8
	s_add_u32 s64, s56, s19
	s_addc_u32 s65, s57, 0
	v_mov_b32_e32 v14, s62
	v_mov_b32_e32 v15, s63
	v_mov_b32_e32 v22, s64
	v_mov_b32_e32 v23, s65
	v_lshl_add_u64 v[22:23], v[22:23], 0, v[4:5]
	v_mad_u64_u32 v[28:29], vcc, v6, s10, v[22:23]
	s_and_b32 s35, s25, 0x3fffffff
	s_add_i32 s35, s35, 1
	s_cmpk_ge_u32 s35, 0x2620
	s_cselect_b32 s33, 1, 0
	s_mul_i32 s8, s33, 0x2620
	s_sub_u32 s35, s35, s8
	s_cmpk_lt_u32 s35, 0x420
	s_cbranch_scc1 .Lfc_p3_st1_s1_kin
	s_cmpk_lt_u32 s35, 0x520
	s_cbranch_scc1 .Lfc_p3_st1_s1_kout
	s_cmpk_lt_u32 s35, 0x1b20
	s_cbranch_scc1 .Lfc_p3_st1_s1_kgu
	s_sub_u32 s35, s35, 0x1b20
	s_mul_i32 s8, s35, 0xba2f
	s_lshr_b32 s8, s8, 23
	s_mul_i32 s9, s8, 0xb0
	s_sub_u32 s35, s35, s9
	s_lshl_b32 s33, s33, 4
	s_add_i32 s33, s33, s8
	s_lshr_b32 s8, s35, 1
	s_mul_i32 s9, s8, 0xbb
	s_lshr_b32 s9, s9, 11
	s_mul_i32 s18, s9, 11
	s_sub_u32 s8, s8, s18
	s_lshl_b32 s9, s9, 1
	s_and_b32 s35, s35, 1
	s_or_b32 s9, s9, s35
	s_mov_b64 s[62:63], s[44:45]
	s_movk_i32 s2, 0x2000
	s_movk_i32 s10, 0x600
	s_mul_i32 s18, s33, 0xb00000
	s_mul_i32 s19, s8, 0x100000
	s_add_u32 s18, s18, s19
	s_mul_i32 s19, s33, 0x300000
	s_add_u32 s19, s19, 0x1b300000
	s_mul_i32 s35, s9, 0x30000
	s_add_u32 s19, s19, s35
	s_branch .Lfc_p3_st1_s1_kfin

.Lfc_p3_st1_s1_kfin:
	s_lshl_b32 s9, s9, 9
	s_add_u32 s18, s18, s9
	s_add_u32 s62, s62, s18
	s_addc_u32 s63, s63, 0
	s_lshl_b32 s8, s8, 7
	s_add_u32 s19, s19, s8
	s_add_u32 s64, s56, s19
	s_addc_u32 s65, s57, 0
	v_mov_b32_e32 v12, s62
	v_mov_b32_e32 v19, s63
	v_cmp_ne_u32_e32 vcc, 0, v18
	s_nop 1
	v_cndmask_b32_e32 v14, v14, v12, vcc
	v_cndmask_b32_e32 v15, v15, v19, vcc
	v_mov_b32_e32 v22, s64
	v_mov_b32_e32 v23, s65
	v_lshl_add_u64 v[22:23], v[22:23], 0, v[4:5]
	v_mad_u64_u32 v[30:31], vcc, v6, s10, v[22:23]
	v_lshl_add_u64 v[14:15], v[14:15], 0, v[2:3]
	v_mad_u64_u32 v[20:21], vcc, v1, s2, v[14:15]
	global_load_dwordx4 v[48:51], v[20:21], off nt
	v_lshl_add_u64 v[20:21], v[20:21], 0, s[2:3]
	global_load_dwordx4 v[52:55], v[20:21], off nt
	v_lshl_add_u64 v[20:21], v[20:21], 0, s[2:3]
	global_load_dwordx4 v[56:59], v[20:21], off nt
	v_lshl_add_u64 v[20:21], v[20:21], 0, s[2:3]
	global_load_dwordx4 v[60:63], v[20:21], off nt
	v_lshl_add_u64 v[20:21], v[20:21], 0, s[2:3]
	global_load_dwordx4 v[64:67], v[20:21], off nt
	v_lshl_add_u64 v[20:21], v[20:21], 0, s[2:3]
	global_load_dwordx4 v[68:71], v[20:21], off nt
	v_lshl_add_u64 v[20:21], v[20:21], 0, s[2:3]
	global_load_dwordx4 v[72:75], v[20:21], off nt
	v_lshl_add_u64 v[20:21], v[20:21], 0, s[2:3]
	global_load_dwordx4 v[76:79], v[20:21], off nt
	v_lshl_add_u64 v[20:21], v[20:21], 0, s[2:3]
	global_load_dwordx4 v[80:83], v[20:21], off nt
	v_lshl_add_u64 v[20:21], v[20:21], 0, s[2:3]
	global_load_dwordx4 v[84:87], v[20:21], off nt
	v_lshl_add_u64 v[20:21], v[20:21], 0, s[2:3]
	global_load_dwordx4 v[88:91], v[20:21], off nt
	v_lshl_add_u64 v[20:21], v[20:21], 0, s[2:3]
	global_load_dwordx4 v[92:95], v[20:21], off nt
	v_lshl_add_u64 v[20:21], v[20:21], 0, s[2:3]
	global_load_dwordx4 v[96:99], v[20:21], off nt
	v_lshl_add_u64 v[20:21], v[20:21], 0, s[2:3]
	global_load_dwordx4 v[100:103], v[20:21], off nt
	v_lshl_add_u64 v[20:21], v[20:21], 0, s[2:3]
	global_load_dwordx4 v[104:107], v[20:21], off nt
	v_lshl_add_u64 v[20:21], v[20:21], 0, s[2:3]
	global_load_dwordx4 v[108:111], v[20:21], off nt
	s_waitcnt vmcnt(16)
	s_branch .Lfc_p3_st1_cvt

.Lfc_p3_st1_cvt:
	v_pk_mul_f32 v[112:113], v[112:113], v[8:9]
	v_pk_mul_f32 v[114:115], v[114:115], v[8:9]
	v_pk_mul_f32 v[116:117], v[116:117], v[8:9]
	v_pk_mul_f32 v[118:119], v[118:119], v[8:9]
	v_cvt_pk_fp8_f32 v112, v112, v116
	v_cvt_pk_fp8_f32 v113, v113, v117
	v_cvt_pk_fp8_f32 v114, v114, v118
	v_cvt_pk_fp8_f32 v115, v115, v119
	ds_write_b16 v16, v112 offset:33792
	ds_write_b16 v16, v113 offset:38016
	ds_write_b16 v16, v114 offset:42240
	ds_write_b16 v16, v115 offset:46464
	v_pk_mul_f32 v[120:121], v[120:121], v[8:9]
	v_pk_mul_f32 v[122:123], v[122:123], v[8:9]
	v_pk_mul_f32 v[124:125], v[124:125], v[8:9]
	v_pk_mul_f32 v[126:127], v[126:127], v[8:9]
	v_cvt_pk_fp8_f32 v120, v120, v124
	v_cvt_pk_fp8_f32 v121, v121, v125
	v_cvt_pk_fp8_f32 v122, v122, v126
	v_cvt_pk_fp8_f32 v123, v123, v127
	ds_write_b16 v16, v120 offset:33794
	ds_write_b16 v16, v121 offset:38018
	ds_write_b16 v16, v122 offset:42242
	ds_write_b16 v16, v123 offset:46466
	v_pk_mul_f32 v[128:129], v[128:129], v[8:9]
	v_pk_mul_f32 v[130:131], v[130:131], v[8:9]
	v_pk_mul_f32 v[132:133], v[132:133], v[8:9]
	v_pk_mul_f32 v[134:135], v[134:135], v[8:9]
	v_cvt_pk_fp8_f32 v128, v128, v132
	v_cvt_pk_fp8_f32 v129, v129, v133
	v_cvt_pk_fp8_f32 v130, v130, v134
	v_cvt_pk_fp8_f32 v131, v131, v135
	ds_write_b16 v16, v128 offset:33796
	ds_write_b16 v16, v129 offset:38020
	ds_write_b16 v16, v130 offset:42244
	ds_write_b16 v16, v131 offset:46468
	v_pk_mul_f32 v[136:137], v[136:137], v[8:9]
	v_pk_mul_f32 v[138:139], v[138:139], v[8:9]
	v_pk_mul_f32 v[140:141], v[140:141], v[8:9]
	v_pk_mul_f32 v[142:143], v[142:143], v[8:9]
	v_cvt_pk_fp8_f32 v136, v136, v140
	v_cvt_pk_fp8_f32 v137, v137, v141
	v_cvt_pk_fp8_f32 v138, v138, v142
	v_cvt_pk_fp8_f32 v139, v139, v143
	ds_write_b16 v16, v136 offset:33798
	ds_write_b16 v16, v137 offset:38022
	ds_write_b16 v16, v138 offset:42246
	ds_write_b16 v16, v139 offset:46470
	v_pk_mul_f32 v[144:145], v[144:145], v[8:9]
	v_pk_mul_f32 v[146:147], v[146:147], v[8:9]
	v_pk_mul_f32 v[148:149], v[148:149], v[8:9]
	v_pk_mul_f32 v[150:151], v[150:151], v[8:9]
	v_cvt_pk_fp8_f32 v144, v144, v148
	v_cvt_pk_fp8_f32 v145, v145, v149
	v_cvt_pk_fp8_f32 v146, v146, v150
	v_cvt_pk_fp8_f32 v147, v147, v151
	ds_write_b16 v16, v144 offset:33800
	ds_write_b16 v16, v145 offset:38024
	ds_write_b16 v16, v146 offset:42248
	ds_write_b16 v16, v147 offset:46472
	v_pk_mul_f32 v[152:153], v[152:153], v[8:9]
	v_pk_mul_f32 v[154:155], v[154:155], v[8:9]
	v_pk_mul_f32 v[156:157], v[156:157], v[8:9]
	v_pk_mul_f32 v[158:159], v[158:159], v[8:9]
	v_cvt_pk_fp8_f32 v152, v152, v156
	v_cvt_pk_fp8_f32 v153, v153, v157
	v_cvt_pk_fp8_f32 v154, v154, v158
	v_cvt_pk_fp8_f32 v155, v155, v159
	ds_write_b16 v16, v152 offset:33802
	ds_write_b16 v16, v153 offset:38026
	ds_write_b16 v16, v154 offset:42250
	ds_write_b16 v16, v155 offset:46474
	v_pk_mul_f32 v[160:161], v[160:161], v[8:9]
	v_pk_mul_f32 v[162:163], v[162:163], v[8:9]
	v_pk_mul_f32 v[164:165], v[164:165], v[8:9]
	v_pk_mul_f32 v[166:167], v[166:167], v[8:9]
	v_cvt_pk_fp8_f32 v160, v160, v164
	v_cvt_pk_fp8_f32 v161, v161, v165
	v_cvt_pk_fp8_f32 v162, v162, v166
	v_cvt_pk_fp8_f32 v163, v163, v167
	ds_write_b16 v16, v160 offset:33804
	ds_write_b16 v16, v161 offset:38028
	ds_write_b16 v16, v162 offset:42252
	ds_write_b16 v16, v163 offset:46476
	v_pk_mul_f32 v[168:169], v[168:169], v[8:9]
	v_pk_mul_f32 v[170:171], v[170:171], v[8:9]
	v_pk_mul_f32 v[172:173], v[172:173], v[8:9]
	v_pk_mul_f32 v[174:175], v[174:175], v[8:9]
	v_cvt_pk_fp8_f32 v168, v168, v172
	v_cvt_pk_fp8_f32 v169, v169, v173
	v_cvt_pk_fp8_f32 v170, v170, v174
	v_cvt_pk_fp8_f32 v171, v171, v175
	ds_write_b16 v16, v168 offset:33806
	ds_write_b16 v16, v169 offset:38030
	ds_write_b16 v16, v170 offset:42254
	ds_write_b16 v16, v171 offset:46478
	v_cmp_eq_u32_e32 vcc, 0, v0
	s_and_saveexec_b64 s[16:17], vcc
	s_cbranch_execz .Lfc_p3_st1_slot_done
	s_mov_b32 s33, -1
	s_cmp_lt_i32 s25, 0
	s_cbranch_scc1 .Lfc_p3_st1_slot_w
	s_bitcmp1_b32 s25, 30
	s_cbranch_scc1 .Lfc_p3_st1_slot_w
	v_readfirstlane_b32 s35, v10
	v_readfirstlane_b32 s8, v11
	s_cmpk_ge_u32 s35, 0x4c40
	s_cbranch_scc1 .Lfc_p3_st1_slot_w
	s_cmp_ge_u32 s8, s13
	s_cselect_b32 s8, 0x40000000, 0
	s_or_b32 s33, s35, s8

.Lfc_p3_st1_slot_done:
	s_or_b64 exec, exec, s[16:17]
	s_waitcnt lgkmcnt(0)
	s_barrier
	ds_read_b32 v12, v13 offset:4
	v_add_u32_e32 v176, 0x8400, v17
	ds_read2_b32 v[178:179], v176 offset0:0 offset1:1
	ds_read2_b32 v[180:181], v176 offset0:2 offset1:3
	ds_read2_b32 v[182:183], v176 offset0:4 offset1:5
	ds_read2_b32 v[184:185], v176 offset0:6 offset1:7
	v_add_u32_e32 v186, 0xc600, v17
	ds_read2_b32 v[36:37], v186 offset0:0 offset1:1
	ds_read2_b32 v[38:39], v186 offset0:2 offset1:3
	ds_read2_b32 v[40:41], v186 offset0:4 offset1:5
	ds_read2_b32 v[42:43], v186 offset0:6 offset1:7
	s_waitcnt lgkmcnt(4)
	global_store_dwordx4 v[32:33], v[178:181], off
	global_store_dwordx4 v[32:33], v[182:185], off offset:16
	s_waitcnt lgkmcnt(0)
	global_store_dwordx4 v[34:35], v[36:39], off
	global_store_dwordx4 v[34:35], v[40:43], off offset:16
	s_waitcnt lgkmcnt(0)
	s_mov_b32 s14, s25
	v_readfirstlane_b32 s25, v12
	s_cmp_lt_i32 s14, 0
	s_cbranch_scc1 .Lfc_p3_exit
	s_branch .Lfc_p3_top
